# attention work queues: unit class order changed from R7..R0,S7..S0 to a longest-first interleave of stick-breaking and retention units (S7,S6,S5,S4,S3,R7,S2,R6,...)
# baseline (speedup 1.0000x reference)
; #define LAS __attribute__((address_space(3)))
; DI int tidx() { const int w = __builtin_amdgcn_readfirstlane(((volatile LAS int*)(131072 + 3072))[hw_wave_slot()]); int ln; asm volatile("v_mbcnt_lo_u32_b32 %0, -1, 0\n\tv_mbcnt_hi_u32_b32 %0, -1, %0" : "=v"(ln)); return (w << 6) + ln; }
; __device__ __forceinline__ unsigned xb_ld(unsigned* p)              { return __hip_atomic_load(p, __ATOMIC_RELAXED, __HIP_MEMORY_SCOPE_AGENT); }
; template <int l>
; DI void layer_body(LAS unsigned char* lds, const XcdBarrier& bar, const int lo, const int hi, const int G, const int vcu) {
;     ...
;         if (IN(pb + 1)) {
;             PHASE_WS();
;             const bf16 *RQ = H5, *RK = H5 + SLOT, *RG = H5 + 2 * SLOT, *SQ = H5 + 3 * SLOT, *SK = H5 + 4 * SLOT, *RG1 = (const bf16*)(ws + WS_RG1);
;             LAS int* uq = (LAS int*)(lds + LDSCTL_OFF + 2048);
;             unsigned* qctr = (unsigned*)(ws + WS_CTL) + (size_t)(kargs()->li * DEPTH + l) * 8 * 32;
;             const int q0 = bid & 7;
;             for (;;) {
;                 if (tidx() < 64) {
;                     const int ln = (int)tidx();
;                     const unsigned cnt = (ln < 8) ? xb_ld(qctr + ((q0 + ln) & 7) * 32) : 64u;
;                     unsigned long long m = __ballot(cnt < 64u);
;                     int got = -1, gq = 0;
;                     while (m != 0ull) {
;                         const int j = __builtin_ctzll(m); m &= m - 1ull;
;                         const int qj = (q0 + j) & 7; unsigned t = 0u;
;                         if (ln == 0) t = atomicAdd(qctr + qj * 32, 1u);
;                         t = (unsigned)__builtin_amdgcn_readfirstlane((int)t);
;                         if (t < 64u) { got = (int)t; gq = qj; break; }
;                     }
;                     if (ln == 0) { uq[0] = got; uq[1] = gq; }
;                 }
;                 __syncthreads();
;                 const int u = __builtin_amdgcn_readfirstlane(uq[0]), q = __builtin_amdgcn_readfirstlane(uq[1]);
;                 __syncthreads();
;                 if (u < 0) break;
;                 const int code = (int)((0x89ABCDEF01234567ull >> (4 * (u >> 2))) & 15ull);
;                 const int bh = q * 4 + (u & 3), b = bh >> 3, h = bh & 7, qb = code & 7;
;                 if (code & 8) att::unit<1>(lds, SQ, SK, VT, RG, RG1, O, b, h, qb);
;                 else att::unit<0>(lds, RQ, RK, VT, RG, RG1, O, b, h, qb);
.LBB0_359:
	s_cmp_lt_i32 s78, 3
	s_cselect_b64 s[40:41], -1, 0
	s_and_b64 s[4:5], s[40:41], s[4:5]
	s_andn2_b64 vcc, exec, s[4:5]
	s_cbranch_vccnz .LBB0_416
	s_mov_b64 s[4:5], s[0:1]
	s_load_dwordx2 s[42:43], s[4:5], 0xb0
	s_mov_b64 s[4:5], s[0:1]
	s_load_dword s3, s[4:5], 0xc0
	s_mov_b32 s64, 0x6a7bcdef
	s_waitcnt lgkmcnt(0)
	s_add_u32 s44, s42, 0x18b00000
	s_addc_u32 s45, s43, 0
	s_add_u32 s46, s42, 0x19b00000
	s_addc_u32 s47, s43, 0
	s_add_u32 s48, s42, 0x1ab00000
	s_addc_u32 s49, s43, 0
	s_add_u32 s50, s42, 0x1bb00000
	s_addc_u32 s51, s43, 0
	s_add_u32 s52, s42, 0x1cb00000
	s_addc_u32 s53, s43, 0
	s_add_u32 s54, s42, 0x68300000
	s_addc_u32 s55, s43, 0
	s_lshl_b32 s4, s3, 1
	s_ashr_i32 s5, s4, 31
	s_lshl_b64 s[4:5], s[4:5], 10
	s_add_u32 s56, s42, s4
	s_addc_u32 s57, s43, s5
	s_add_u32 s58, s42, 0x1db00000
	s_addc_u32 s59, s43, 0
	s_add_u32 s60, s42, 0x23b00000
	s_addc_u32 s61, s43, 0
	s_add_i32 s3, 0, 0x20800
	v_mbcnt_lo_u32_b32 v0, -1, 0
	s_mov_b32 s63, 0
	s_mov_b32 s65, 0x8123945
	v_mov_b32_e32 v145, 0
	s_movk_i32 s35, 0x110
	s_movk_i32 s39, 0x88
	s_mov_b32 s79, 0xc2fc0000
	s_mov_b32 s80, 0xc3160000
	s_mov_b64 s[66:67], 0x23b00800
	s_mov_b32 s81, 0x23b00000
	s_mov_b32 s82, 0x20000
	s_mov_b64 s[68:69], 0x1db00180
	s_mov_b64 s[70:71], 0x100
	s_mov_b64 s[72:73], 0x40000
	s_add_i32 s83, 0, 0x12000
	v_mov_b32_e32 v147, 0x41d80000
	s_mov_b32 s84, 0x5040100
	v_mov_b32_e32 v192, 0x3727c5ac
	s_mov_b32 s85, 0xf800000
	v_mov_b32_e32 v193, 0x260
	v_mov_b32_e32 v194, s3
	v_mbcnt_hi_u32_b32 v195, -1, v0
	v_mov_b32_e32 v196, 0x42fc0000
	v_mov_b32_e32 v197, 0x42800000
	s_branch .LBB0_363

; #define LAS __attribute__((address_space(3)))
; DI int tidx() { const int w = __builtin_amdgcn_readfirstlane(((volatile LAS int*)(131072 + 3072))[hw_wave_slot()]); int ln; asm volatile("v_mbcnt_lo_u32_b32 %0, -1, 0\n\tv_mbcnt_hi_u32_b32 %0, -1, %0" : "=v"(ln)); return (w << 6) + ln; }
; __device__ __forceinline__ unsigned xb_ld(unsigned* p)              { return __hip_atomic_load(p, __ATOMIC_RELAXED, __HIP_MEMORY_SCOPE_AGENT); }
; template <int l>
; DI void layer_body(LAS unsigned char* lds, const XcdBarrier& bar, const int lo, const int hi, const int G, const int vcu) {
;     ...
;         if (IN(pb + 1)) {
;             PHASE_WS();
;             const bf16 *RQ = H5, *RK = H5 + SLOT, *RG = H5 + 2 * SLOT, *SQ = H5 + 3 * SLOT, *SK = H5 + 4 * SLOT, *RG1 = (const bf16*)(ws + WS_RG1);
;             LAS int* uq = (LAS int*)(lds + LDSCTL_OFF + 2048);
;             unsigned* qctr = (unsigned*)(ws + WS_CTL) + (size_t)(kargs()->li * DEPTH + l) * 8 * 32;
;             const int q0 = bid & 7;
;             for (;;) {
;                 if (tidx() < 64) {
;                     const int ln = (int)tidx();
;                     const unsigned cnt = (ln < 8) ? xb_ld(qctr + ((q0 + ln) & 7) * 32) : 64u;
;                     unsigned long long m = __ballot(cnt < 64u);
;                     int got = -1, gq = 0;
;                     while (m != 0ull) {
;                         const int j = __builtin_ctzll(m); m &= m - 1ull;
;                         const int qj = (q0 + j) & 7; unsigned t = 0u;
;                         if (ln == 0) t = atomicAdd(qctr + qj * 32, 1u);
;                         t = (unsigned)__builtin_amdgcn_readfirstlane((int)t);
;                         if (t < 64u) { got = (int)t; gq = qj; break; }
;                     }
;                     if (ln == 0) { uq[0] = got; uq[1] = gq; }
;                 }
;                 __syncthreads();
;                 const int u = __builtin_amdgcn_readfirstlane(uq[0]), q = __builtin_amdgcn_readfirstlane(uq[1]);
;                 __syncthreads();
;                 if (u < 0) break;
;                 const int code = (int)((0x89ABCDEF01234567ull >> (4 * (u >> 2))) & 15ull);
;                 const int bh = q * 4 + (u & 3), b = bh >> 3, h = bh & 7, qb = code & 7;
;                 if (code & 8) att::unit<1>(lds, SQ, SK, VT, RG, RG1, O, b, h, qb);
;                 else att::unit<0>(lds, RQ, RK, VT, RG, RG1, O, b, h, qb);
.LBB0_1095:
	s_cmp_lt_i32 s78, 12
	s_cselect_b64 s[40:41], -1, 0
	s_and_b64 s[4:5], s[40:41], s[4:5]
	s_andn2_b64 vcc, exec, s[4:5]
	s_cbranch_vccnz .LBB0_1152
	s_mov_b64 s[4:5], s[0:1]
	s_load_dwordx2 s[42:43], s[4:5], 0xb0
	s_mov_b64 s[4:5], s[0:1]
	s_load_dword s3, s[4:5], 0xc0
	s_mov_b32 s64, 0x6a7bcdef
	s_waitcnt lgkmcnt(0)
	s_add_u32 s44, s42, 0x18b00000
	s_addc_u32 s45, s43, 0
	s_add_u32 s46, s42, 0x19b00000
	s_addc_u32 s47, s43, 0
	s_add_u32 s48, s42, 0x1ab00000
	s_addc_u32 s49, s43, 0
	s_add_u32 s50, s42, 0x1bb00000
	s_addc_u32 s51, s43, 0
	s_add_u32 s52, s42, 0x1cb00000
	s_addc_u32 s53, s43, 0
	s_add_u32 s54, s42, 0x68300000
	s_addc_u32 s55, s43, 0
	s_lshl_b32 s3, s3, 1
	s_or_b32 s4, s3, 1
	s_ashr_i32 s5, s4, 31
	s_lshl_b64 s[4:5], s[4:5], 10
	s_add_u32 s56, s42, s4
	s_addc_u32 s57, s43, s5
	s_add_u32 s58, s42, 0x1db00000
	s_addc_u32 s59, s43, 0
	s_add_u32 s60, s42, 0x23b00000
	s_addc_u32 s61, s43, 0
	s_add_i32 s3, 0, 0x20800
	v_mbcnt_lo_u32_b32 v0, -1, 0
	s_mov_b32 s63, 0
	s_mov_b32 s65, 0x8123945
	v_mov_b32_e32 v145, 0
	s_movk_i32 s35, 0x110
	s_movk_i32 s39, 0x88
	s_mov_b32 s79, 0xc2fc0000
	s_mov_b32 s80, 0xc3160000
	s_mov_b64 s[66:67], 0x23b00800
	s_mov_b32 s81, 0x23b00000
	s_mov_b32 s82, 0x20000
	s_mov_b64 s[68:69], 0x1db00180
	s_mov_b64 s[70:71], 0x100
	s_mov_b64 s[72:73], 0x40000
	s_add_i32 s83, 0, 0x12000
	v_mov_b32_e32 v147, 0x41d80000
	s_mov_b32 s84, 0x5040100
	v_mov_b32_e32 v192, 0x3727c5ac
	s_mov_b32 s85, 0xf800000
	v_mov_b32_e32 v193, 0x260
	v_mov_b32_e32 v194, s3
	v_mbcnt_hi_u32_b32 v195, -1, v0
	v_mov_b32_e32 v196, 0x42fc0000
	v_mov_b32_e32 v197, 0x42800000
	s_branch .LBB0_1099
